# speedup vs baseline: 1.0239x; 1.0239x over previous
.Lno_karg_touch:
	v_mul_f32_e32 v16, v12, v12
	v_add_f32_e32 v17, 0x3f800000, v12
	v_add_f32_e32 v18, 0x40000000, v12
	v_add_f32_e32 v19, 0x40400000, v12
	v_mul_f32_e32 v17, v17, v17
	v_mul_f32_e32 v18, v18, v18
	v_mul_f32_e32 v19, v19, v19
	v_mul_f32_e32 v20, v8, v16
	v_mul_f32_e32 v24, v9, v16
	v_mul_f32_e32 v21, v8, v17
	v_mul_f32_e32 v25, v9, v17
	v_mul_f32_e32 v22, v8, v18
	v_mul_f32_e32 v26, v9, v18
	v_mul_f32_e32 v23, v8, v19
	v_mul_f32_e32 v27, v9, v19
	v_exp_f32_e32 v20, v20
	v_exp_f32_e32 v21, v21
	v_exp_f32_e32 v22, v22
	v_exp_f32_e32 v23, v23
	v_exp_f32_e32 v24, v24
	v_exp_f32_e32 v25, v25
	v_exp_f32_e32 v26, v26
	v_exp_f32_e32 v27, v27
	v_cvt_pk_f16_f32 v32, v20, v21
	v_cvt_pk_f16_f32 v33, v22, v23
	v_cvt_pk_f16_f32 v64, v24, v25
	v_cvt_pk_f16_f32 v65, v26, v27
	v_add_f32_e32 v16, 0x40800000, v12
	v_add_f32_e32 v17, 0x40a00000, v12
	v_add_f32_e32 v18, 0x40c00000, v12
	v_add_f32_e32 v19, 0x40e00000, v12
	v_mul_f32_e32 v16, v16, v16
	v_mul_f32_e32 v17, v17, v17
	v_mul_f32_e32 v18, v18, v18
	v_mul_f32_e32 v19, v19, v19
	v_mul_f32_e32 v20, v8, v16
	v_mul_f32_e32 v24, v9, v16
	v_mul_f32_e32 v21, v8, v17
	v_mul_f32_e32 v25, v9, v17
	v_mul_f32_e32 v22, v8, v18
	v_mul_f32_e32 v26, v9, v18
	v_mul_f32_e32 v23, v8, v19
	v_mul_f32_e32 v27, v9, v19
	v_exp_f32_e32 v20, v20
	v_exp_f32_e32 v21, v21
	v_exp_f32_e32 v22, v22
	v_exp_f32_e32 v23, v23
	v_exp_f32_e32 v24, v24
	v_exp_f32_e32 v25, v25
	v_exp_f32_e32 v26, v26
	v_exp_f32_e32 v27, v27
	v_cvt_pk_f16_f32 v34, v20, v21
	v_cvt_pk_f16_f32 v35, v22, v23
	v_cvt_pk_f16_f32 v66, v24, v25
	v_cvt_pk_f16_f32 v67, v26, v27
	v_add_f32_e32 v16, 0x42000000, v12
	v_add_f32_e32 v17, 0x42040000, v12
	v_add_f32_e32 v18, 0x42080000, v12
	v_add_f32_e32 v19, 0x420c0000, v12
	v_mul_f32_e32 v16, v16, v16
	v_mul_f32_e32 v17, v17, v17
	v_mul_f32_e32 v18, v18, v18
	v_mul_f32_e32 v19, v19, v19
	v_mul_f32_e32 v20, v8, v16
	v_mul_f32_e32 v24, v9, v16
	v_mul_f32_e32 v21, v8, v17
	v_mul_f32_e32 v25, v9, v17
	v_mul_f32_e32 v22, v8, v18
	v_mul_f32_e32 v26, v9, v18
	v_mul_f32_e32 v23, v8, v19
	v_mul_f32_e32 v27, v9, v19
	v_exp_f32_e32 v20, v20
	v_exp_f32_e32 v21, v21
	v_exp_f32_e32 v22, v22
	v_exp_f32_e32 v23, v23
	v_exp_f32_e32 v24, v24
	v_exp_f32_e32 v25, v25
	v_exp_f32_e32 v26, v26
	v_exp_f32_e32 v27, v27
	v_cvt_pk_f16_f32 v36, v20, v21
	v_cvt_pk_f16_f32 v37, v22, v23
	v_cvt_pk_f16_f32 v68, v24, v25
	v_cvt_pk_f16_f32 v69, v26, v27
	v_add_f32_e32 v16, 0x42100000, v12
	v_add_f32_e32 v17, 0x42140000, v12
	v_add_f32_e32 v18, 0x42180000, v12
	v_add_f32_e32 v19, 0x421c0000, v12
	v_mul_f32_e32 v16, v16, v16
	v_mul_f32_e32 v17, v17, v17
	v_mul_f32_e32 v18, v18, v18
	v_mul_f32_e32 v19, v19, v19
	v_mul_f32_e32 v20, v8, v16
	v_mul_f32_e32 v24, v9, v16
	v_mul_f32_e32 v21, v8, v17
	v_mul_f32_e32 v25, v9, v17
	v_mul_f32_e32 v22, v8, v18
	v_mul_f32_e32 v26, v9, v18
	v_mul_f32_e32 v23, v8, v19
	v_mul_f32_e32 v27, v9, v19
	v_exp_f32_e32 v20, v20
	v_exp_f32_e32 v21, v21
	v_exp_f32_e32 v22, v22
	v_exp_f32_e32 v23, v23
	v_exp_f32_e32 v24, v24
	v_exp_f32_e32 v25, v25
	v_exp_f32_e32 v26, v26
	v_exp_f32_e32 v27, v27
	v_cvt_pk_f16_f32 v38, v20, v21
	v_cvt_pk_f16_f32 v39, v22, v23
	v_cvt_pk_f16_f32 v70, v24, v25
	v_cvt_pk_f16_f32 v71, v26, v27
	v_add_u32_e32 v6, 0x8000, v6
	global_load_dwordx4 v[160:163], v6, s[12:13] offset:0 nt
	global_load_dwordx4 v[164:167], v6, s[12:13] offset:1024 nt
	global_load_dwordx4 v[168:171], v6, s[12:13] offset:2048 nt
	global_load_dwordx4 v[172:175], v6, s[12:13] offset:3072 nt
	v_add_f32_e32 v16, 0x42800000, v12
	v_add_f32_e32 v17, 0x42820000, v12
	v_add_f32_e32 v18, 0x42840000, v12
	v_add_f32_e32 v19, 0x42860000, v12
	v_mul_f32_e32 v16, v16, v16
	v_mul_f32_e32 v17, v17, v17
	v_mul_f32_e32 v18, v18, v18
	v_mul_f32_e32 v19, v19, v19
	v_mul_f32_e32 v20, v8, v16
	v_mul_f32_e32 v24, v9, v16
	v_mul_f32_e32 v21, v8, v17
	v_mul_f32_e32 v25, v9, v17
	v_mul_f32_e32 v22, v8, v18
	v_mul_f32_e32 v26, v9, v18
	v_mul_f32_e32 v23, v8, v19
	v_mul_f32_e32 v27, v9, v19
	v_exp_f32_e32 v20, v20
	v_exp_f32_e32 v21, v21
	v_exp_f32_e32 v22, v22
	v_exp_f32_e32 v23, v23
	v_exp_f32_e32 v24, v24
	v_exp_f32_e32 v25, v25
	v_exp_f32_e32 v26, v26
	v_exp_f32_e32 v27, v27
	v_cvt_pk_f16_f32 v40, v20, v21
	v_cvt_pk_f16_f32 v41, v22, v23
	v_cvt_pk_f16_f32 v72, v24, v25
	v_cvt_pk_f16_f32 v73, v26, v27
	v_add_f32_e32 v16, 0x42880000, v12
	v_add_f32_e32 v17, 0x428a0000, v12
	v_add_f32_e32 v18, 0x428c0000, v12
	v_add_f32_e32 v19, 0x428e0000, v12
	v_mul_f32_e32 v16, v16, v16
	v_mul_f32_e32 v17, v17, v17
	v_mul_f32_e32 v18, v18, v18
	v_mul_f32_e32 v19, v19, v19
	v_mul_f32_e32 v20, v8, v16
	v_mul_f32_e32 v24, v9, v16
	v_mul_f32_e32 v21, v8, v17
	v_mul_f32_e32 v25, v9, v17
	v_mul_f32_e32 v22, v8, v18
	v_mul_f32_e32 v26, v9, v18
	v_mul_f32_e32 v23, v8, v19
	v_mul_f32_e32 v27, v9, v19
	v_exp_f32_e32 v20, v20
	v_exp_f32_e32 v21, v21
	v_exp_f32_e32 v22, v22
	v_exp_f32_e32 v23, v23
	v_exp_f32_e32 v24, v24
	v_exp_f32_e32 v25, v25
	v_exp_f32_e32 v26, v26
	v_exp_f32_e32 v27, v27
	v_cvt_pk_f16_f32 v42, v20, v21
	v_cvt_pk_f16_f32 v43, v22, v23
	v_cvt_pk_f16_f32 v74, v24, v25
	v_cvt_pk_f16_f32 v75, v26, v27
	v_add_f32_e32 v16, 0x42c00000, v12
	v_add_f32_e32 v17, 0x42c20000, v12
	v_add_f32_e32 v18, 0x42c40000, v12
	v_add_f32_e32 v19, 0x42c60000, v12
	v_mul_f32_e32 v16, v16, v16
	v_mul_f32_e32 v17, v17, v17
	v_mul_f32_e32 v18, v18, v18
	v_mul_f32_e32 v19, v19, v19
	v_mul_f32_e32 v20, v8, v16
	v_mul_f32_e32 v24, v9, v16
	v_mul_f32_e32 v21, v8, v17
	v_mul_f32_e32 v25, v9, v17
	v_mul_f32_e32 v22, v8, v18
	v_mul_f32_e32 v26, v9, v18
	v_mul_f32_e32 v23, v8, v19
	v_mul_f32_e32 v27, v9, v19
	v_exp_f32_e32 v20, v20
	v_exp_f32_e32 v21, v21
	v_exp_f32_e32 v22, v22
	v_exp_f32_e32 v23, v23
	v_exp_f32_e32 v24, v24
	v_exp_f32_e32 v25, v25
	v_exp_f32_e32 v26, v26
	v_exp_f32_e32 v27, v27
	v_cvt_pk_f16_f32 v44, v20, v21
	v_cvt_pk_f16_f32 v45, v22, v23
	v_cvt_pk_f16_f32 v76, v24, v25
	v_cvt_pk_f16_f32 v77, v26, v27
	v_add_f32_e32 v16, 0x42c80000, v12
	v_add_f32_e32 v17, 0x42ca0000, v12
	v_add_f32_e32 v18, 0x42cc0000, v12
	v_add_f32_e32 v19, 0x42ce0000, v12
	v_mul_f32_e32 v16, v16, v16
	v_mul_f32_e32 v17, v17, v17
	v_mul_f32_e32 v18, v18, v18
	v_mul_f32_e32 v19, v19, v19
	v_mul_f32_e32 v20, v8, v16
	v_mul_f32_e32 v24, v9, v16
	v_mul_f32_e32 v21, v8, v17
	v_mul_f32_e32 v25, v9, v17
	v_mul_f32_e32 v22, v8, v18
	v_mul_f32_e32 v26, v9, v18
	v_mul_f32_e32 v23, v8, v19
	v_mul_f32_e32 v27, v9, v19
	v_exp_f32_e32 v20, v20
	v_exp_f32_e32 v21, v21
	v_exp_f32_e32 v22, v22
	v_exp_f32_e32 v23, v23
	v_exp_f32_e32 v24, v24
	v_exp_f32_e32 v25, v25
	v_exp_f32_e32 v26, v26
	v_exp_f32_e32 v27, v27
	v_cvt_pk_f16_f32 v46, v20, v21
	v_cvt_pk_f16_f32 v47, v22, v23
	v_cvt_pk_f16_f32 v78, v24, v25
	v_cvt_pk_f16_f32 v79, v26, v27
	v_add_u32_e32 v6, 0x8000, v6
	global_load_dwordx4 v[176:179], v6, s[12:13] offset:0 nt
	global_load_dwordx4 v[180:183], v6, s[12:13] offset:1024 nt
	global_load_dwordx4 v[184:187], v6, s[12:13] offset:2048 nt
	global_load_dwordx4 v[188:191], v6, s[12:13] offset:3072 nt
	v_mul_f32_e32 v16, v2, v2
	v_add_f32_e32 v17, 0x3f800000, v2
	v_add_f32_e32 v18, 0x40000000, v2
	v_add_f32_e32 v19, 0x40400000, v2
	v_mul_f32_e32 v17, v17, v17
	v_mul_f32_e32 v18, v18, v18
	v_mul_f32_e32 v19, v19, v19
	v_mul_f32_e32 v20, v28, v16
	v_mul_f32_e32 v24, v29, v16
	v_mul_f32_e32 v21, v28, v17
	v_mul_f32_e32 v25, v29, v17
	v_mul_f32_e32 v22, v28, v18
	v_mul_f32_e32 v26, v29, v18
	v_mul_f32_e32 v23, v28, v19
	v_mul_f32_e32 v27, v29, v19
	v_exp_f32_e32 v20, v20
	v_exp_f32_e32 v21, v21
	v_exp_f32_e32 v22, v22
	v_exp_f32_e32 v23, v23
	v_exp_f32_e32 v24, v24
	v_exp_f32_e32 v25, v25
	v_exp_f32_e32 v26, v26
	v_exp_f32_e32 v27, v27
	v_cvt_pk_f16_f32 v48, v20, v21
	v_cvt_pk_f16_f32 v49, v22, v23
	v_cvt_pk_f16_f32 v80, v24, v25
	v_cvt_pk_f16_f32 v81, v26, v27
	v_add_f32_e32 v16, 0x40800000, v2
	v_add_f32_e32 v17, 0x40a00000, v2
	v_add_f32_e32 v18, 0x40c00000, v2
	v_add_f32_e32 v19, 0x40e00000, v2
	v_mul_f32_e32 v16, v16, v16
	v_mul_f32_e32 v17, v17, v17
	v_mul_f32_e32 v18, v18, v18
	v_mul_f32_e32 v19, v19, v19
	v_mul_f32_e32 v20, v28, v16
	v_mul_f32_e32 v24, v29, v16
	v_mul_f32_e32 v21, v28, v17
	v_mul_f32_e32 v25, v29, v17
	v_mul_f32_e32 v22, v28, v18
	v_mul_f32_e32 v26, v29, v18
	v_mul_f32_e32 v23, v28, v19
	v_mul_f32_e32 v27, v29, v19
	v_exp_f32_e32 v20, v20
	v_exp_f32_e32 v21, v21
	v_exp_f32_e32 v22, v22
	v_exp_f32_e32 v23, v23
	v_exp_f32_e32 v24, v24
	v_exp_f32_e32 v25, v25
	v_exp_f32_e32 v26, v26
	v_exp_f32_e32 v27, v27
	v_cvt_pk_f16_f32 v50, v20, v21
	v_cvt_pk_f16_f32 v51, v22, v23
	v_cvt_pk_f16_f32 v82, v24, v25
	v_cvt_pk_f16_f32 v83, v26, v27
	v_add_f32_e32 v16, 0x42000000, v2
	v_add_f32_e32 v17, 0x42040000, v2
	v_add_f32_e32 v18, 0x42080000, v2
	v_add_f32_e32 v19, 0x420c0000, v2
	v_mul_f32_e32 v16, v16, v16
	v_mul_f32_e32 v17, v17, v17
	v_mul_f32_e32 v18, v18, v18
	v_mul_f32_e32 v19, v19, v19
	v_mul_f32_e32 v20, v28, v16
	v_mul_f32_e32 v24, v29, v16
	v_mul_f32_e32 v21, v28, v17
	v_mul_f32_e32 v25, v29, v17
	v_mul_f32_e32 v22, v28, v18
	v_mul_f32_e32 v26, v29, v18
	v_mul_f32_e32 v23, v28, v19
	v_mul_f32_e32 v27, v29, v19
	v_exp_f32_e32 v20, v20
	v_exp_f32_e32 v21, v21
	v_exp_f32_e32 v22, v22
	v_exp_f32_e32 v23, v23
	v_exp_f32_e32 v24, v24
	v_exp_f32_e32 v25, v25
	v_exp_f32_e32 v26, v26
	v_exp_f32_e32 v27, v27
	v_cvt_pk_f16_f32 v52, v20, v21
	v_cvt_pk_f16_f32 v53, v22, v23
	v_cvt_pk_f16_f32 v84, v24, v25
	v_cvt_pk_f16_f32 v85, v26, v27
	v_add_f32_e32 v16, 0x42100000, v2
	v_add_f32_e32 v17, 0x42140000, v2
	v_add_f32_e32 v18, 0x42180000, v2
	v_add_f32_e32 v19, 0x421c0000, v2
	v_mul_f32_e32 v16, v16, v16
	v_mul_f32_e32 v17, v17, v17
	v_mul_f32_e32 v18, v18, v18
	v_mul_f32_e32 v19, v19, v19
	v_mul_f32_e32 v20, v28, v16
	v_mul_f32_e32 v24, v29, v16
	v_mul_f32_e32 v21, v28, v17
	v_mul_f32_e32 v25, v29, v17
	v_mul_f32_e32 v22, v28, v18
	v_mul_f32_e32 v26, v29, v18
	v_mul_f32_e32 v23, v28, v19
	v_mul_f32_e32 v27, v29, v19
	v_exp_f32_e32 v20, v20
	v_exp_f32_e32 v21, v21
	v_exp_f32_e32 v22, v22
	v_exp_f32_e32 v23, v23
	v_exp_f32_e32 v24, v24
	v_exp_f32_e32 v25, v25
	v_exp_f32_e32 v26, v26
	v_exp_f32_e32 v27, v27
	v_cvt_pk_f16_f32 v54, v20, v21
	v_cvt_pk_f16_f32 v55, v22, v23
	v_cvt_pk_f16_f32 v86, v24, v25
	v_cvt_pk_f16_f32 v87, v26, v27
	v_add_u32_e32 v6, 0x8000, v6
	global_load_dwordx4 v[192:195], v6, s[12:13] offset:0 nt
	global_load_dwordx4 v[196:199], v6, s[12:13] offset:1024 nt
	global_load_dwordx4 v[200:203], v6, s[12:13] offset:2048 nt
	global_load_dwordx4 v[204:207], v6, s[12:13] offset:3072 nt
	v_add_f32_e32 v16, 0x42800000, v2
	v_add_f32_e32 v17, 0x42820000, v2
	v_add_f32_e32 v18, 0x42840000, v2
	v_add_f32_e32 v19, 0x42860000, v2
	v_mul_f32_e32 v16, v16, v16
	v_mul_f32_e32 v17, v17, v17
	v_mul_f32_e32 v18, v18, v18
	v_mul_f32_e32 v19, v19, v19
	v_mul_f32_e32 v20, v28, v16
	v_mul_f32_e32 v24, v29, v16
	v_mul_f32_e32 v21, v28, v17
	v_mul_f32_e32 v25, v29, v17
	v_mul_f32_e32 v22, v28, v18
	v_mul_f32_e32 v26, v29, v18
	v_mul_f32_e32 v23, v28, v19
	v_mul_f32_e32 v27, v29, v19
	v_exp_f32_e32 v20, v20
	v_exp_f32_e32 v21, v21
	v_exp_f32_e32 v22, v22
	v_exp_f32_e32 v23, v23
	v_exp_f32_e32 v24, v24
	v_exp_f32_e32 v25, v25
	v_exp_f32_e32 v26, v26
	v_exp_f32_e32 v27, v27
	v_cvt_pk_f16_f32 v56, v20, v21
	v_cvt_pk_f16_f32 v57, v22, v23
	v_cvt_pk_f16_f32 v88, v24, v25
	v_cvt_pk_f16_f32 v89, v26, v27
	v_add_f32_e32 v16, 0x42880000, v2
	v_add_f32_e32 v17, 0x428a0000, v2
	v_add_f32_e32 v18, 0x428c0000, v2
	v_add_f32_e32 v19, 0x428e0000, v2
	v_mul_f32_e32 v16, v16, v16
	v_mul_f32_e32 v17, v17, v17
	v_mul_f32_e32 v18, v18, v18
	v_mul_f32_e32 v19, v19, v19
	v_mul_f32_e32 v20, v28, v16
	v_mul_f32_e32 v24, v29, v16
	v_mul_f32_e32 v21, v28, v17
	v_mul_f32_e32 v25, v29, v17
	v_mul_f32_e32 v22, v28, v18
	v_mul_f32_e32 v26, v29, v18
	v_mul_f32_e32 v23, v28, v19
	v_mul_f32_e32 v27, v29, v19
	v_exp_f32_e32 v20, v20
	v_exp_f32_e32 v21, v21
	v_exp_f32_e32 v22, v22
	v_exp_f32_e32 v23, v23
	v_exp_f32_e32 v24, v24
	v_exp_f32_e32 v25, v25
	v_exp_f32_e32 v26, v26
	v_exp_f32_e32 v27, v27
	v_cvt_pk_f16_f32 v58, v20, v21
	v_cvt_pk_f16_f32 v59, v22, v23
	v_cvt_pk_f16_f32 v90, v24, v25
	v_cvt_pk_f16_f32 v91, v26, v27
	v_add_f32_e32 v16, 0x42c00000, v2
	v_add_f32_e32 v17, 0x42c20000, v2
	v_add_f32_e32 v18, 0x42c40000, v2
	v_add_f32_e32 v19, 0x42c60000, v2
	v_mul_f32_e32 v16, v16, v16
	v_mul_f32_e32 v17, v17, v17
	v_mul_f32_e32 v18, v18, v18
	v_mul_f32_e32 v19, v19, v19
	v_mul_f32_e32 v20, v28, v16
	v_mul_f32_e32 v24, v29, v16
	v_mul_f32_e32 v21, v28, v17
	v_mul_f32_e32 v25, v29, v17
	v_mul_f32_e32 v22, v28, v18
	v_mul_f32_e32 v26, v29, v18
	v_mul_f32_e32 v23, v28, v19
	v_mul_f32_e32 v27, v29, v19
	v_exp_f32_e32 v20, v20
	v_exp_f32_e32 v21, v21
	v_exp_f32_e32 v22, v22
	v_exp_f32_e32 v23, v23
	v_exp_f32_e32 v24, v24
	v_exp_f32_e32 v25, v25
	v_exp_f32_e32 v26, v26
	v_exp_f32_e32 v27, v27
	v_cvt_pk_f16_f32 v60, v20, v21
	v_cvt_pk_f16_f32 v61, v22, v23
	v_cvt_pk_f16_f32 v92, v24, v25
	v_cvt_pk_f16_f32 v93, v26, v27
	v_add_f32_e32 v16, 0x42c80000, v2
	v_add_f32_e32 v17, 0x42ca0000, v2
	v_add_f32_e32 v18, 0x42cc0000, v2
	v_add_f32_e32 v19, 0x42ce0000, v2
	v_mul_f32_e32 v16, v16, v16
	v_mul_f32_e32 v17, v17, v17
	v_mul_f32_e32 v18, v18, v18
	v_mul_f32_e32 v19, v19, v19
	v_mul_f32_e32 v20, v28, v16
	v_mul_f32_e32 v24, v29, v16
	v_mul_f32_e32 v21, v28, v17
	v_mul_f32_e32 v25, v29, v17
	v_mul_f32_e32 v22, v28, v18
	v_mul_f32_e32 v26, v29, v18
	v_mul_f32_e32 v23, v28, v19
	v_mul_f32_e32 v27, v29, v19
	v_exp_f32_e32 v20, v20
	v_exp_f32_e32 v21, v21
	v_exp_f32_e32 v22, v22
	v_exp_f32_e32 v23, v23
	v_exp_f32_e32 v24, v24
	v_exp_f32_e32 v25, v25
	v_exp_f32_e32 v26, v26
	v_exp_f32_e32 v27, v27
	v_cvt_pk_f16_f32 v62, v20, v21
	v_cvt_pk_f16_f32 v63, v22, v23
	v_cvt_pk_f16_f32 v94, v24, v25
	v_cvt_pk_f16_f32 v95, v26, v27
	v_add_u32_e32 v6, 0x8000, v6
	global_load_dwordx4 v[208:211], v6, s[12:13] offset:0 nt
	global_load_dwordx4 v[212:215], v6, s[12:13] offset:1024 nt
	global_load_dwordx4 v[216:219], v6, s[12:13] offset:2048 nt
	global_load_dwordx4 v[220:223], v6, s[12:13] offset:3072 nt
	v_mul_f32_e32 v16, v13, v13
	v_add_f32_e32 v17, 0x3f800000, v13
	v_add_f32_e32 v18, 0x40000000, v13
	v_add_f32_e32 v19, 0x40400000, v13
	v_mul_f32_e32 v17, v17, v17
	v_mul_f32_e32 v18, v18, v18
	v_mul_f32_e32 v19, v19, v19
	v_mul_f32_e32 v20, v8, v16
	v_mul_f32_e32 v24, v9, v16
	v_mul_f32_e32 v21, v8, v17
	v_mul_f32_e32 v25, v9, v17
	v_mul_f32_e32 v22, v8, v18
	v_mul_f32_e32 v26, v9, v18
	v_mul_f32_e32 v23, v8, v19
	v_mul_f32_e32 v27, v9, v19
	v_exp_f32_e32 v20, v20
	v_exp_f32_e32 v21, v21
	v_exp_f32_e32 v22, v22
	v_exp_f32_e32 v23, v23
	v_exp_f32_e32 v24, v24
	v_exp_f32_e32 v25, v25
	v_exp_f32_e32 v26, v26
	v_exp_f32_e32 v27, v27
	v_mul_f32_e32 v96, v10, v20
	v_mul_f32_e32 v97, v10, v21
	v_mul_f32_e32 v98, v10, v22
	v_mul_f32_e32 v99, v10, v23
	v_mul_f32_e32 v112, v11, v24
	v_mul_f32_e32 v113, v11, v25
	v_mul_f32_e32 v114, v11, v26
	v_mul_f32_e32 v115, v11, v27
	v_add_u32_e32 v6, 0x8000, v6
	global_load_dwordx4 v[224:227], v6, s[12:13] offset:0 nt
	global_load_dwordx4 v[228:231], v6, s[12:13] offset:1024 nt
	global_load_dwordx4 v[232:235], v6, s[12:13] offset:2048 nt
	global_load_dwordx4 v[236:239], v6, s[12:13] offset:3072 nt
	v_add_f32_e32 v16, 0x41800000, v13
	v_add_f32_e32 v17, 0x41880000, v13
	v_add_f32_e32 v18, 0x41900000, v13
	v_add_f32_e32 v19, 0x41980000, v13
	v_mul_f32_e32 v16, v16, v16
	v_mul_f32_e32 v17, v17, v17
	v_mul_f32_e32 v18, v18, v18
	v_mul_f32_e32 v19, v19, v19
	v_mul_f32_e32 v20, v8, v16
	v_mul_f32_e32 v24, v9, v16
	v_mul_f32_e32 v21, v8, v17
	v_mul_f32_e32 v25, v9, v17
	v_mul_f32_e32 v22, v8, v18
	v_mul_f32_e32 v26, v9, v18
	v_mul_f32_e32 v23, v8, v19
	v_mul_f32_e32 v27, v9, v19
	v_exp_f32_e32 v20, v20
	v_exp_f32_e32 v21, v21
	v_exp_f32_e32 v22, v22
	v_exp_f32_e32 v23, v23
	v_exp_f32_e32 v24, v24
	v_exp_f32_e32 v25, v25
	v_exp_f32_e32 v26, v26
	v_exp_f32_e32 v27, v27
	v_mul_f32_e32 v100, v10, v20
	v_mul_f32_e32 v101, v10, v21
	v_mul_f32_e32 v102, v10, v22
	v_mul_f32_e32 v103, v10, v23
	v_mul_f32_e32 v116, v11, v24
	v_mul_f32_e32 v117, v11, v25
	v_mul_f32_e32 v118, v11, v26
	v_mul_f32_e32 v119, v11, v27
	v_add_u32_e32 v6, 0x8000, v6
	global_load_dwordx4 v[240:243], v6, s[12:13] offset:0 nt
	global_load_dwordx4 v[244:247], v6, s[12:13] offset:1024 nt
	global_load_dwordx4 v[248:251], v6, s[12:13] offset:2048 nt
	global_load_dwordx4 v[252:255], v6, s[12:13] offset:3072 nt
	v_mul_f32_e32 v16, v3, v3
	v_add_f32_e32 v17, 0x3f800000, v3
	v_add_f32_e32 v18, 0x40000000, v3
	v_add_f32_e32 v19, 0x40400000, v3
	v_mul_f32_e32 v17, v17, v17
	v_mul_f32_e32 v18, v18, v18
	v_mul_f32_e32 v19, v19, v19
	v_mul_f32_e32 v20, v28, v16
	v_mul_f32_e32 v24, v29, v16
	v_mul_f32_e32 v21, v28, v17
	v_mul_f32_e32 v25, v29, v17
	v_mul_f32_e32 v22, v28, v18
	v_mul_f32_e32 v26, v29, v18
	v_mul_f32_e32 v23, v28, v19
	v_mul_f32_e32 v27, v29, v19
	v_exp_f32_e32 v20, v20
	v_exp_f32_e32 v21, v21
	v_exp_f32_e32 v22, v22
	v_exp_f32_e32 v23, v23
	v_exp_f32_e32 v24, v24
	v_exp_f32_e32 v25, v25
	v_exp_f32_e32 v26, v26
	v_exp_f32_e32 v27, v27
	v_mul_f32_e32 v104, v30, v20
	v_mul_f32_e32 v105, v30, v21
	v_mul_f32_e32 v106, v30, v22
	v_mul_f32_e32 v107, v30, v23
	v_mul_f32_e32 v120, v31, v24
	v_mul_f32_e32 v121, v31, v25
	v_mul_f32_e32 v122, v31, v26
	v_mul_f32_e32 v123, v31, v27
	v_add_f32_e32 v16, 0x41800000, v3
	v_add_f32_e32 v17, 0x41880000, v3
	v_add_f32_e32 v18, 0x41900000, v3
	v_add_f32_e32 v19, 0x41980000, v3
	v_mul_f32_e32 v16, v16, v16
	v_mul_f32_e32 v17, v17, v17
	v_mul_f32_e32 v18, v18, v18
	v_mul_f32_e32 v19, v19, v19
	v_mul_f32_e32 v20, v28, v16
	v_mul_f32_e32 v24, v29, v16
	v_mul_f32_e32 v21, v28, v17
	v_mul_f32_e32 v25, v29, v17
	v_mul_f32_e32 v22, v28, v18
	v_mul_f32_e32 v26, v29, v18
	v_mul_f32_e32 v23, v28, v19
	v_mul_f32_e32 v27, v29, v19
	v_exp_f32_e32 v20, v20
	v_exp_f32_e32 v21, v21
	v_exp_f32_e32 v22, v22
	v_exp_f32_e32 v23, v23
	v_exp_f32_e32 v24, v24
	v_exp_f32_e32 v25, v25
	v_exp_f32_e32 v26, v26
	v_exp_f32_e32 v27, v27
	v_mul_f32_e32 v108, v30, v20
	v_mul_f32_e32 v109, v30, v21
	v_mul_f32_e32 v110, v30, v22
	v_mul_f32_e32 v111, v30, v23
	v_mul_f32_e32 v124, v31, v24
	v_mul_f32_e32 v125, v31, v25
	v_mul_f32_e32 v126, v31, v26
	v_mul_f32_e32 v127, v31, v27
	s_waitcnt vmcnt(28)
	v_add_f32_e32 v128, v128, v129
	v_add_f32_e32 v130, v130, v131
	v_add_f32_e32 v132, v132, v133
	v_add_f32_e32 v134, v134, v135
	v_add_f32_e32 v136, v136, v137
	v_add_f32_e32 v138, v138, v139
	v_add_f32_e32 v140, v140, v141
	v_add_f32_e32 v142, v142, v143
	v_add_f32_e32 v128, v128, v130
	v_add_f32_e32 v132, v132, v134
	v_add_f32_e32 v136, v136, v138
	v_add_f32_e32 v140, v140, v142
	v_cndmask_b32_e64 v130, v128, v132, s[30:31]
	v_cndmask_b32_e64 v134, v136, v140, s[30:31]
	v_cndmask_b32_e64 v129, v132, v128, s[30:31]
	v_cndmask_b32_e64 v133, v140, v136, s[30:31]
	v_add_f32_dpp v129, v130, v129 quad_perm:[1,0,3,2] row_mask:0xf bank_mask:0xf bound_ctrl:1
	v_add_f32_dpp v133, v134, v133 quad_perm:[1,0,3,2] row_mask:0xf bank_mask:0xf bound_ctrl:1
	v_cndmask_b32_e64 v135, v129, v133, s[32:33]
	v_cndmask_b32_e64 v131, v133, v129, s[32:33]
	s_nop 1
	v_add_f32_dpp v131, v135, v131 quad_perm:[2,3,0,1] row_mask:0xf bank_mask:0xf bound_ctrl:1
	v_cvt_f16_f32_e32 v131, v131
	ds_write_b16 v14, v131 offset:0
	s_waitcnt vmcnt(24)
	v_add_f32_e32 v144, v144, v145
	v_add_f32_e32 v146, v146, v147
	v_add_f32_e32 v148, v148, v149
	v_add_f32_e32 v150, v150, v151
	v_add_f32_e32 v152, v152, v153
	v_add_f32_e32 v154, v154, v155
	v_add_f32_e32 v156, v156, v157
	v_add_f32_e32 v158, v158, v159
	v_add_f32_e32 v144, v144, v146
	v_add_f32_e32 v148, v148, v150
	v_add_f32_e32 v152, v152, v154
	v_add_f32_e32 v156, v156, v158
	v_cndmask_b32_e64 v146, v144, v148, s[30:31]
	v_cndmask_b32_e64 v150, v152, v156, s[30:31]
	v_cndmask_b32_e64 v145, v148, v144, s[30:31]
	v_cndmask_b32_e64 v149, v156, v152, s[30:31]
	v_add_f32_dpp v145, v146, v145 quad_perm:[1,0,3,2] row_mask:0xf bank_mask:0xf bound_ctrl:1
	v_add_f32_dpp v149, v150, v149 quad_perm:[1,0,3,2] row_mask:0xf bank_mask:0xf bound_ctrl:1
	v_cndmask_b32_e64 v151, v145, v149, s[32:33]
	v_cndmask_b32_e64 v147, v149, v145, s[32:33]
	s_nop 1
	v_add_f32_dpp v147, v151, v147 quad_perm:[2,3,0,1] row_mask:0xf bank_mask:0xf bound_ctrl:1
	v_cvt_f16_f32_e32 v147, v147
	ds_write_b16 v14, v147 offset:1088
	s_waitcnt vmcnt(20)
	v_add_f32_e32 v160, v160, v161
	v_add_f32_e32 v162, v162, v163
	v_add_f32_e32 v164, v164, v165
	v_add_f32_e32 v166, v166, v167
	v_add_f32_e32 v168, v168, v169
	v_add_f32_e32 v170, v170, v171
	v_add_f32_e32 v172, v172, v173
	v_add_f32_e32 v174, v174, v175
	v_add_f32_e32 v160, v160, v162
	v_add_f32_e32 v164, v164, v166
	v_add_f32_e32 v168, v168, v170
	v_add_f32_e32 v172, v172, v174
	v_cndmask_b32_e64 v162, v160, v164, s[30:31]
	v_cndmask_b32_e64 v166, v168, v172, s[30:31]
	v_cndmask_b32_e64 v161, v164, v160, s[30:31]
	v_cndmask_b32_e64 v165, v172, v168, s[30:31]
	v_add_f32_dpp v161, v162, v161 quad_perm:[1,0,3,2] row_mask:0xf bank_mask:0xf bound_ctrl:1
	v_add_f32_dpp v165, v166, v165 quad_perm:[1,0,3,2] row_mask:0xf bank_mask:0xf bound_ctrl:1
	v_cndmask_b32_e64 v167, v161, v165, s[32:33]
	v_cndmask_b32_e64 v163, v165, v161, s[32:33]
	s_nop 1
	v_add_f32_dpp v163, v167, v163 quad_perm:[2,3,0,1] row_mask:0xf bank_mask:0xf bound_ctrl:1
	v_cvt_f16_f32_e32 v163, v163
	ds_write_b16 v14, v163 offset:2176
	s_waitcnt vmcnt(16)
	v_add_f32_e32 v176, v176, v177
	v_add_f32_e32 v178, v178, v179
	v_add_f32_e32 v180, v180, v181
	v_add_f32_e32 v182, v182, v183
	v_add_f32_e32 v184, v184, v185
	v_add_f32_e32 v186, v186, v187
	v_add_f32_e32 v188, v188, v189
	v_add_f32_e32 v190, v190, v191
	v_add_f32_e32 v176, v176, v178
	v_add_f32_e32 v180, v180, v182
	v_add_f32_e32 v184, v184, v186
	v_add_f32_e32 v188, v188, v190
	v_cndmask_b32_e64 v178, v176, v180, s[30:31]
	v_cndmask_b32_e64 v182, v184, v188, s[30:31]
	v_cndmask_b32_e64 v177, v180, v176, s[30:31]
	v_cndmask_b32_e64 v181, v188, v184, s[30:31]
	v_add_f32_dpp v177, v178, v177 quad_perm:[1,0,3,2] row_mask:0xf bank_mask:0xf bound_ctrl:1
	v_add_f32_dpp v181, v182, v181 quad_perm:[1,0,3,2] row_mask:0xf bank_mask:0xf bound_ctrl:1
	v_cndmask_b32_e64 v183, v177, v181, s[32:33]
	v_cndmask_b32_e64 v179, v181, v177, s[32:33]
	s_nop 1
	v_add_f32_dpp v179, v183, v179 quad_perm:[2,3,0,1] row_mask:0xf bank_mask:0xf bound_ctrl:1
	v_cvt_f16_f32_e32 v179, v179
	ds_write_b16 v14, v179 offset:3264
	s_mov_b32 s29, 0
	v_mov_b32_e32 v160, 0
	v_mov_b32_e32 v161, 0
	v_mov_b32_e32 v162, 0
	v_mov_b32_e32 v163, 0
	s_lshl_b32 s6, s6, 6
	s_add_i32 s6, s6, s7
	s_lshl_b32 s6, s6, 10
	v_add_u32_e32 v5, s6, v5
	s_branch .Lpass
